# final RMSNorm: all 16 loads of a row in flight together instead of 8 serialised load-wait-store chunks
# speedup vs baseline: 1.0072x; 1.0035x over previous
; #define WS_FRESH() GAS unsigned char* wsg_ = (GAS unsigned char*)ws0; asm volatile("" : "+s"(wsg_)); unsigned char* ws = (unsigned char*)wsg_
; #define FRESH_TID() int ftid; asm volatile("v_mbcnt_lo_u32_b32 %0, -1, 0\n\tv_mbcnt_hi_u32_b32 %0, -1, %0" : "=v"(ftid)); ftid += (wave << 6); const int flane = ftid & 63; (void)flane
; __global__ void __launch_bounds__(NWAVES * 64, 2) mk_fwd(Args args) {
;     ...
;     { WS_FRESH(); FRESH_TID(); const int lane = flane;
;     for (int t = gw; t < T; t += NGW) {
;         float sv = lane < 32 ? W_ss[(size_t)t * 32 + lane] : 0.f; sv = wave_sum(sv);
;         const float rstd = 1.0f / sqrtf(sv * (1.0f / D) + EPS);
; #pragma unroll
;         for (int c = lane * 4; c < D; c += 256) { const u32x2 q_ = *(const u32x2*)(W_x + XIDX(t, c)); const f32x4 g = *(const f32x4*)(final_g + c);
;             const f32x4 v = {__builtin_bit_cast(float, q_.x << 16), __builtin_bit_cast(float, q_.x & 0xFFFF0000u), __builtin_bit_cast(float, q_.y << 16), __builtin_bit_cast(float, q_.y & 0xFFFF0000u)};
;             *(f32x4*)(args.out + (size_t)t * D + c) = v * rstd * g; }
.LBB0_1473:
	s_or_b64 exec, exec, s[2:3]
	s_ashr_i32 s12, s86, 3
	s_andn2_b32 s12, s12, 31
	s_and_b32 s2, s10, 0x3fc0
	s_lshl_b32 s2, s2, 1
	s_add_u32 s6, s8, s2
	s_addc_u32 s7, s9, 0
	v_or_b32_e32 v44, s12, v33
	v_ashrrev_i32_e32 v45, 31, v44
	v_lshlrev_b64 v[44:45], 15, v[44:45]
	v_lshl_add_u64 v[44:45], s[6:7], 0, v[44:45]
	v_lshl_add_u64 v[44:45], v[44:45], 0, v[14:15]
	global_load_dwordx2 v[56:57], v[44:45], off
	v_or_b32_e32 v44, s12, v34
	v_ashrrev_i32_e32 v45, 31, v44
	v_lshlrev_b64 v[44:45], 15, v[44:45]
	v_lshl_add_u64 v[44:45], s[6:7], 0, v[44:45]
	v_lshl_add_u64 v[44:45], v[44:45], 0, v[14:15]
	global_load_dwordx2 v[58:59], v[44:45], off
	v_or_b32_e32 v44, s12, v35
	v_ashrrev_i32_e32 v45, 31, v44
	v_lshlrev_b64 v[44:45], 15, v[44:45]
	v_lshl_add_u64 v[44:45], s[6:7], 0, v[44:45]
	v_lshl_add_u64 v[44:45], v[44:45], 0, v[14:15]
	global_load_dwordx2 v[60:61], v[44:45], off
	v_or_b32_e32 v44, s12, v36
	v_ashrrev_i32_e32 v45, 31, v44
	v_lshlrev_b64 v[44:45], 15, v[44:45]
	v_lshl_add_u64 v[44:45], s[6:7], 0, v[44:45]
	v_lshl_add_u64 v[44:45], v[44:45], 0, v[14:15]
	global_load_dwordx2 v[62:63], v[44:45], off
	v_or_b32_e32 v44, s12, v37
	v_ashrrev_i32_e32 v45, 31, v44
	v_lshlrev_b64 v[44:45], 15, v[44:45]
	v_lshl_add_u64 v[44:45], s[6:7], 0, v[44:45]
	v_lshl_add_u64 v[44:45], v[44:45], 0, v[14:15]
	global_load_dwordx2 v[64:65], v[44:45], off
	v_or_b32_e32 v44, s12, v38
	v_ashrrev_i32_e32 v45, 31, v44
	v_lshlrev_b64 v[44:45], 15, v[44:45]
	v_lshl_add_u64 v[44:45], s[6:7], 0, v[44:45]
	v_lshl_add_u64 v[44:45], v[44:45], 0, v[14:15]
	global_load_dwordx2 v[66:67], v[44:45], off
	v_or_b32_e32 v44, s12, v39
	v_ashrrev_i32_e32 v45, 31, v44
	v_lshlrev_b64 v[44:45], 15, v[44:45]
	v_lshl_add_u64 v[44:45], s[6:7], 0, v[44:45]
	v_lshl_add_u64 v[44:45], v[44:45], 0, v[14:15]
	global_load_dwordx2 v[68:69], v[44:45], off
	v_or_b32_e32 v44, s12, v40
	v_ashrrev_i32_e32 v45, 31, v44
	v_lshlrev_b64 v[44:45], 15, v[44:45]
	v_lshl_add_u64 v[44:45], s[6:7], 0, v[44:45]
	v_lshl_add_u64 v[44:45], v[44:45], 0, v[14:15]
	global_load_dwordx2 v[70:71], v[44:45], off
	global_load_dwordx4 v[72:75], v[2:3], off
	global_load_dwordx4 v[76:79], v[2:3], off offset:1024
	global_load_dwordx4 v[80:83], v[2:3], off offset:2048
	global_load_dwordx4 v[84:87], v[2:3], off offset:3072
	global_load_dwordx4 v[88:91], v[4:5], off
	global_load_dwordx4 v[92:95], v[6:7], off
	global_load_dwordx4 v[96:99], v[8:9], off
	global_load_dwordx4 v[100:103], v[10:11], off
	s_waitcnt vmcnt(16)
	ds_bpermute_b32 v23, v27, v21
	v_readlane_b32 s16, v250, 37
	v_or_b32_e32 v52, s12, v34
	v_lshlrev_b64 v[24:25], 13, v[24:25]
	v_readlane_b32 s17, v250, 38
	s_waitcnt lgkmcnt(0)
	v_add_f32_e32 v21, v21, v23
	ds_bpermute_b32 v23, v28, v21
	v_ashrrev_i32_e32 v53, 31, v52
	v_lshl_add_u64 v[24:25], s[16:17], 0, v[24:25]
	v_lshlrev_b64 v[52:53], 15, v[52:53]
	v_lshl_add_u64 v[48:49], v[24:25], 0, v[16:17]
	s_waitcnt lgkmcnt(0)
	v_add_f32_e32 v21, v21, v23
	ds_bpermute_b32 v23, v29, v21
	v_lshl_add_u64 v[52:53], s[6:7], 0, v[52:53]
	v_lshl_add_u64 v[52:53], v[52:53], 0, v[14:15]
	v_lshl_add_u64 v[12:13], v[12:13], 0, s[4:5]
	v_readlane_b32 s18, v250, 39
	s_waitcnt lgkmcnt(0)
	v_add_f32_e32 v21, v21, v23
	ds_bpermute_b32 v23, v30, v21
	v_readlane_b32 s19, v250, 40
	s_waitcnt lgkmcnt(0)
	v_add_f32_e32 v21, v21, v23
	ds_bpermute_b32 v23, v31, v21
	s_waitcnt lgkmcnt(0)
	v_add_f32_e32 v21, v21, v23
	ds_bpermute_b32 v23, v32, v21
	s_waitcnt lgkmcnt(0)
; __global__ void __launch_bounds__(NWAVES * 64, 2) mk_fwd(Args args) {
;     ...
;     for (int t = gw; t < T; t += NGW) {
;         float sv = lane < 32 ? W_ss[(size_t)t * 32 + lane] : 0.f; sv = wave_sum(sv);
;         const float rstd = 1.0f / sqrtf(sv * (1.0f / D) + EPS);
; #pragma unroll
;         for (int c = lane * 4; c < D; c += 256) { const u32x2 q_ = *(const u32x2*)(W_x + XIDX(t, c)); const f32x4 g = *(const f32x4*)(final_g + c);
;             const f32x4 v = {__builtin_bit_cast(float, q_.x << 16), __builtin_bit_cast(float, q_.x & 0xFFFF0000u), __builtin_bit_cast(float, q_.y << 16), __builtin_bit_cast(float, q_.y & 0xFFFF0000u)};
;             *(f32x4*)(args.out + (size_t)t * D + c) = v * rstd * g; }
	v_add_f32_e32 v21, v21, v23
	v_fmamk_f32 v21, v21, 0x3a000000, v41
	v_mul_f32_e32 v23, 0x4f800000, v21
	v_cmp_gt_f32_e32 vcc, s11, v21
	s_nop 1
	v_cndmask_b32_e32 v21, v21, v23, vcc
	v_sqrt_f32_e32 v23, v21
	s_nop 0
	v_add_u32_e32 v26, -1, v23
	v_add_u32_e32 v43, 1, v23
	v_fma_f32 v54, -v26, v23, v21
	v_fma_f32 v55, -v43, v23, v21
	v_cmp_ge_f32_e64 s[2:3], 0, v54
	s_nop 1
	v_cndmask_b32_e64 v23, v23, v26, s[2:3]
	v_cmp_lt_f32_e64 s[2:3], 0, v55
	s_nop 1
	v_cndmask_b32_e64 v23, v23, v43, s[2:3]
	v_mul_f32_e32 v26, 0x37800000, v23
	v_cndmask_b32_e32 v23, v23, v26, vcc
	v_cmp_class_f32_e32 vcc, v21, v42
	s_nop 1
	v_cndmask_b32_e32 v21, v23, v21, vcc
	v_div_scale_f32 v23, s[2:3], v21, v21, 1.0
	v_rcp_f32_e32 v26, v23
	v_div_scale_f32 v43, vcc, 1.0, v21, 1.0
	s_mov_b64 s[2:3], s[14:15]
	v_fma_f32 v54, -v23, v26, 1.0
	v_fmac_f32_e32 v26, v54, v26
	v_mul_f32_e32 v54, v43, v26
	v_fma_f32 v55, -v23, v54, v43
	v_fmac_f32_e32 v54, v55, v26
	v_fma_f32 v23, -v23, v54, v43
	v_div_fmas_f32 v23, v23, v26, v54
	v_div_fixup_f32 v26, v23, v21, 1.0
	v_mov_b32_e32 v21, v1
	s_add_u32 s86, s86, s2
	v_readlane_b32 s2, v251, 7
	v_mov_b32_e32 v23, v1
	s_addc_u32 s87, s87, s3
	s_add_i32 s10, s10, s2
	s_cmpk_gt_i32 s86, 0x1fff
	s_waitcnt vmcnt(0)
	v_lshlrev_b32_e32 v54, 16, v56
	v_and_b32_e32 v55, 0xffff0000, v56
	v_lshlrev_b32_e32 v50, 16, v57
	v_and_b32_e32 v51, 0xffff0000, v57
	v_pk_mul_f32 v[54:55], v[26:27], v[54:55] op_sel_hi:[0,1]
	v_pk_mul_f32 v[50:51], v[26:27], v[50:51] op_sel_hi:[0,1]
	v_pk_mul_f32 v[46:47], v[74:75], v[50:51]
	v_pk_mul_f32 v[44:45], v[72:73], v[54:55]
	global_store_dwordx4 v[48:49], v[44:47], off
	v_lshlrev_b32_e32 v54, 16, v58
	v_and_b32_e32 v55, 0xffff0000, v58
	v_lshlrev_b32_e32 v50, 16, v59
	v_and_b32_e32 v51, 0xffff0000, v59
	v_pk_mul_f32 v[54:55], v[26:27], v[54:55] op_sel_hi:[0,1]
	v_pk_mul_f32 v[50:51], v[26:27], v[50:51] op_sel_hi:[0,1]
	v_pk_mul_f32 v[46:47], v[78:79], v[50:51]
	v_pk_mul_f32 v[44:45], v[76:77], v[54:55]
	global_store_dwordx4 v[48:49], v[44:47], off offset:1024
	v_lshlrev_b32_e32 v54, 16, v60
	v_and_b32_e32 v55, 0xffff0000, v60
	v_lshlrev_b32_e32 v50, 16, v61
	v_and_b32_e32 v51, 0xffff0000, v61
	v_pk_mul_f32 v[54:55], v[26:27], v[54:55] op_sel_hi:[0,1]
	v_pk_mul_f32 v[50:51], v[26:27], v[50:51] op_sel_hi:[0,1]
	v_pk_mul_f32 v[46:47], v[82:83], v[50:51]
	v_pk_mul_f32 v[44:45], v[80:81], v[54:55]
	global_store_dwordx4 v[48:49], v[44:47], off offset:2048
	v_lshlrev_b32_e32 v54, 16, v62
	v_and_b32_e32 v55, 0xffff0000, v62
	v_lshlrev_b32_e32 v50, 16, v63
	v_and_b32_e32 v51, 0xffff0000, v63
	v_pk_mul_f32 v[54:55], v[26:27], v[54:55] op_sel_hi:[0,1]
	v_pk_mul_f32 v[50:51], v[26:27], v[50:51] op_sel_hi:[0,1]
	v_pk_mul_f32 v[46:47], v[86:87], v[50:51]
	v_pk_mul_f32 v[44:45], v[84:85], v[54:55]
	global_store_dwordx4 v[48:49], v[44:47], off offset:3072
	v_lshlrev_b32_e32 v54, 16, v64
	v_and_b32_e32 v55, 0xffff0000, v64
	v_lshlrev_b32_e32 v50, 16, v65
	v_and_b32_e32 v51, 0xffff0000, v65
	v_pk_mul_f32 v[54:55], v[26:27], v[54:55] op_sel_hi:[0,1]
	v_pk_mul_f32 v[50:51], v[26:27], v[50:51] op_sel_hi:[0,1]
	v_pk_mul_f32 v[46:47], v[90:91], v[50:51]
	v_pk_mul_f32 v[44:45], v[88:89], v[54:55]
	v_lshl_add_u64 v[52:53], v[24:25], 0, v[18:19]
	global_store_dwordx4 v[52:53], v[44:47], off
	v_lshlrev_b32_e32 v54, 16, v66
	v_and_b32_e32 v55, 0xffff0000, v66
	v_lshlrev_b32_e32 v50, 16, v67
	v_and_b32_e32 v51, 0xffff0000, v67
	v_pk_mul_f32 v[54:55], v[26:27], v[54:55] op_sel_hi:[0,1]
	v_pk_mul_f32 v[50:51], v[26:27], v[50:51] op_sel_hi:[0,1]
	v_pk_mul_f32 v[46:47], v[94:95], v[50:51]
	v_pk_mul_f32 v[44:45], v[92:93], v[54:55]
	v_lshl_add_u64 v[52:53], v[24:25], 0, v[0:1]
	global_store_dwordx4 v[52:53], v[44:47], off
	v_lshlrev_b32_e32 v54, 16, v68
	v_and_b32_e32 v55, 0xffff0000, v68
	v_lshlrev_b32_e32 v50, 16, v69
	v_and_b32_e32 v51, 0xffff0000, v69
	v_pk_mul_f32 v[54:55], v[26:27], v[54:55] op_sel_hi:[0,1]
	v_pk_mul_f32 v[50:51], v[26:27], v[50:51] op_sel_hi:[0,1]
	v_pk_mul_f32 v[46:47], v[98:99], v[50:51]
	v_pk_mul_f32 v[44:45], v[96:97], v[54:55]
	v_lshl_add_u64 v[52:53], v[24:25], 0, v[20:21]
	global_store_dwordx4 v[52:53], v[44:47], off
	v_lshlrev_b32_e32 v54, 16, v70
	v_and_b32_e32 v55, 0xffff0000, v70
	v_lshlrev_b32_e32 v50, 16, v71
	v_and_b32_e32 v51, 0xffff0000, v71
	v_pk_mul_f32 v[54:55], v[26:27], v[54:55] op_sel_hi:[0,1]
	v_pk_mul_f32 v[50:51], v[26:27], v[50:51] op_sel_hi:[0,1]
	v_pk_mul_f32 v[46:47], v[102:103], v[50:51]
	v_pk_mul_f32 v[44:45], v[100:101], v[54:55]
	v_lshl_add_u64 v[52:53], v[24:25], 0, v[22:23]
	global_store_dwordx4 v[52:53], v[44:47], off
	s_cbranch_scc1 .LBB0_1476
